# stack on v004: norm2 modulation loads batched (8 serial round trips to 2), dn_prep wave-0 gate loads waited late, final phase next-row indices prefetched
# speedup vs baseline: 1.0358x; 1.0047x over previous
.LBB0_444:
	s_waitcnt lgkmcnt(0)
	s_barrier
	s_load_dwordx2 s[56:57], s[0:1], 0x58
	s_bfe_u32 s12, s60, 0x20001
	s_lshl_b32 s58, s31, 6
	v_bfrev_b32_e32 v63, 1
	v_mov_b32_e32 v97, 0
	s_waitcnt lgkmcnt(0)
	s_add_u32 s56, s56, s8
	s_addc_u32 s57, s57, s9
	s_lshl_b32 s31, s12, 7
	v_or_b32_e32 v4, s31, v64
	v_add_u32_e32 v2, v4, v65
	v_ashrrev_i32_e32 v3, 31, v2
	v_lshl_add_u64 v[2:3], v[2:3], 2, s[56:57]
	global_load_dword v30, v[2:3], off
	v_add_u32_e32 v2, v4, v66
	v_ashrrev_i32_e32 v3, 31, v2
	v_lshl_add_u64 v[2:3], v[2:3], 2, s[56:57]
	global_load_dword v31, v[2:3], off
	v_add_u32_e32 v2, v4, v67
	v_ashrrev_i32_e32 v3, 31, v2
	v_lshl_add_u64 v[2:3], v[2:3], 2, s[56:57]
	global_load_dword v32, v[2:3], off
	v_cndmask_b32_e64 v3, 0, 1, s[90:91]
	v_mov_b32_e32 v2, 0
	v_cmp_ne_u32_e64 s[56:57], 1, v3
	s_andn2_b64 vcc, exec, s[90:91]
	s_cbranch_vccnz .LBB0_446
	v_sub_u32_e32 v3, 63, v62
	v_readlane_b32 vcc_lo, v254, 58
	v_cndmask_b32_e64 v3, v3, v62, s[38:39]
	v_readlane_b32 vcc_hi, v254, 59
	v_add_u32_e32 v3, s58, v3
	v_readlane_b32 s59, v253, 45
	v_mov_b64_e32 v[4:5], vcc
	v_mad_i64_i32 v[4:5], vcc, v3, s30, v[4:5]
	s_lshl_b32 s68, s59, 1
	s_lshl_b32 vcc_lo, s12, 1
	s_mov_b32 vcc_hi, s69
	v_lshl_add_u64 v[4:5], v[4:5], 0, s[68:69]
	v_lshl_add_u64 v[4:5], v[4:5], 0, vcc
	v_add_co_u32_e32 v4, vcc, 0x2000, v4
	s_nop 1
	v_addc_co_u32_e32 v5, vcc, 0, v5, vcc
	global_load_ushort v246, v[4:5], off offset:1024
	s_nop 0
	global_load_ushort v248, v[4:5], off offset:1040

.LBB0_460:
	s_or_b64 exec, exec, s[10:11]
	s_waitcnt vmcnt(0)
	s_andn2_b64 vcc, exec, s[90:91]
	s_cbranch_vccnz .Ldnp_nogate
	v_lshlrev_b32_e32 v246, 16, v246
	v_lshlrev_b32_e32 v97, 16, v248
	v_mul_f32_e32 v63, 0xbfb8aa3b, v246
.Ldnp_nogate:
	ds_write2st64_b32 v75, v30, v31 offset1:8
	ds_write_b32 v75, v32 offset:4096
	s_and_saveexec_b64 s[10:11], s[40:41]
	s_cbranch_execnz .LBB0_585
	s_or_b64 exec, exec, s[10:11]
	s_and_saveexec_b64 s[10:11], s[42:43]
	s_cbranch_execnz .LBB0_586

.LBB0_1141:
	s_cmp_lt_u32 s13, 4
	s_cselect_b32 s4, s13, s96
	s_cselect_b32 s5, s97, 0x4000
	s_lshl_b32 s17, s4, 4
	s_add_i32 s17, s17, s5
	s_and_b32 s4, s13, 0x7ffffffb
	s_cmp_lg_u32 s4, 0
	s_cbranch_scc1 .LBB0_1143
	s_min_i32 s4, s17, 0x4000
	s_ashr_i32 s4, s4, 12
	s_mul_hi_i32 s5, s4, 0xc000
	s_mul_i32 s4, s4, 0xc000
	s_add_u32 s6, s2, s4
	s_addc_u32 s7, s10, s5
	v_lshl_add_u64 v[74:75], s[6:7], 0, v[98:99]
	s_mov_b64 s[6:7], 0x6000
	s_load_dwordx2 s[4:5], s[0:1], 0x38
	v_lshl_add_u64 v[100:101], v[74:75], 0, s[6:7]
	s_mov_b64 s[6:7], 0x8000
	v_lshl_add_u64 v[102:103], v[74:75], 0, s[6:7]
	s_movk_i32 s6, 0x7000
	v_add_co_u32_e32 v124, vcc, s6, v74
	s_mov_b32 s6, 0x9000
	s_nop 0
	v_addc_co_u32_e32 v125, vcc, 0, v75, vcc
	s_lshl_b64 s[8:9], s[68:69], 2
	v_add_co_u32_e32 v128, vcc, s6, v74
	s_waitcnt lgkmcnt(0)
	s_add_u32 s4, s4, s8
	v_addc_co_u32_e32 v129, vcc, 0, v75, vcc
	s_addc_u32 s5, s5, s9
	v_lshl_add_u64 v[104:105], s[4:5], 0, v[98:99]
	v_add_co_u32_e32 v126, vcc, s58, v104
	s_nop 1
	v_addc_co_u32_e32 v127, vcc, 0, v105, vcc
	v_mov_b64_e32 v[146:147], v[100:101]
	global_load_dwordx4 v[70:73], v98, s[4:5]
	global_load_dwordx4 v[78:81], v98, s[4:5] offset:1024
	global_load_dwordx4 v[86:89], v98, s[4:5] offset:2048
	global_load_dwordx4 v[94:97], v98, s[4:5] offset:3072
	global_load_dwordx4 v[104:107], v[126:127], off
	global_load_dwordx4 v[112:115], v[126:127], off offset:1024
	global_load_dwordx4 v[120:123], v[126:127], off offset:2048
	global_load_dwordx4 v[152:155], v[126:127], off offset:3072
	global_load_dwordx4 v[74:77], v[128:129], off offset:-4096
	global_load_dwordx4 v[82:85], v[102:103], off offset:1024
	global_load_dwordx4 v[90:93], v[102:103], off offset:2048
	global_load_dwordx4 v[108:111], v[128:129], off
	global_load_dwordx4 v[116:119], v[128:129], off offset:1024
	global_load_dwordx4 v[148:151], v[128:129], off offset:2048
	s_nop 0
	global_load_dwordx4 v[100:103], v[102:103], off offset:3072
	s_nop 0
	global_load_dwordx4 v[128:131], v[128:129], off offset:3072
	s_waitcnt vmcnt(0)
	v_pk_add_f32 v[76:77], v[76:77], 1.0 op_sel_hi:[1,0]
	v_pk_add_f32 v[74:75], v[74:75], 1.0 op_sel_hi:[1,0]
	v_pk_mul_f32 v[72:73], v[72:73], v[76:77]
	v_pk_mul_f32 v[70:71], v[70:71], v[74:75]
	v_pk_add_f32 v[84:85], v[84:85], 1.0 op_sel_hi:[1,0]
	v_pk_add_f32 v[82:83], v[82:83], 1.0 op_sel_hi:[1,0]
	v_pk_mul_f32 v[80:81], v[80:81], v[84:85]
	v_pk_mul_f32 v[78:79], v[78:79], v[82:83]
	v_pk_add_f32 v[92:93], v[92:93], 1.0 op_sel_hi:[1,0]
	v_pk_add_f32 v[90:91], v[90:91], 1.0 op_sel_hi:[1,0]
	v_pk_mul_f32 v[88:89], v[88:89], v[92:93]
	v_pk_mul_f32 v[86:87], v[86:87], v[90:91]
	v_pk_add_f32 v[102:103], v[102:103], 1.0 op_sel_hi:[1,0]
	v_pk_add_f32 v[100:101], v[100:101], 1.0 op_sel_hi:[1,0]
	v_pk_mul_f32 v[96:97], v[96:97], v[102:103]
	v_pk_mul_f32 v[94:95], v[94:95], v[100:101]
	v_pk_add_f32 v[110:111], v[110:111], 1.0 op_sel_hi:[1,0]
	v_pk_add_f32 v[108:109], v[108:109], 1.0 op_sel_hi:[1,0]
	v_pk_mul_f32 v[106:107], v[106:107], v[110:111]
	v_pk_mul_f32 v[104:105], v[104:105], v[108:109]
	v_pk_add_f32 v[118:119], v[118:119], 1.0 op_sel_hi:[1,0]
	v_pk_add_f32 v[116:117], v[116:117], 1.0 op_sel_hi:[1,0]
	v_pk_mul_f32 v[114:115], v[114:115], v[118:119]
	v_pk_mul_f32 v[112:113], v[112:113], v[116:117]
	v_pk_add_f32 v[150:151], v[150:151], 1.0 op_sel_hi:[1,0]
	v_pk_add_f32 v[148:149], v[148:149], 1.0 op_sel_hi:[1,0]
	v_pk_mul_f32 v[122:123], v[122:123], v[150:151]
	v_pk_mul_f32 v[120:121], v[120:121], v[148:149]
	v_pk_add_f32 v[130:131], v[130:131], 1.0 op_sel_hi:[1,0]
	v_pk_add_f32 v[128:129], v[128:129], 1.0 op_sel_hi:[1,0]
	v_pk_mul_f32 v[130:131], v[154:155], v[130:131]
	v_pk_mul_f32 v[128:129], v[152:153], v[128:129]
	global_load_dwordx4 v[66:69], v[124:125], off offset:-4096
	global_load_dwordx4 v[74:77], v[146:147], off offset:1024
	global_load_dwordx4 v[82:85], v[146:147], off offset:2048
	global_load_dwordx4 v[90:93], v[146:147], off offset:3072
	global_load_dwordx4 v[100:103], v[124:125], off
	global_load_dwordx4 v[108:111], v[124:125], off offset:1024
	global_load_dwordx4 v[116:119], v[124:125], off offset:2048
	s_nop 0
	global_load_dwordx4 v[124:127], v[124:125], off offset:3072

.LBB0_1567:
	s_cmp_lt_i32 s92, 23
	s_cselect_b64 s[2:3], -1, 0
	s_cmp_gt_i32 s93, 22
	s_cselect_b64 s[4:5], -1, 0
	s_and_b64 s[2:3], s[2:3], s[4:5]
	s_and_b64 vcc, exec, s[2:3]
	s_cbranch_vccz .LBB0_1570
	s_load_dwordx2 s[0:1], s[0:1], 0xe0
	v_readfirstlane_b32 s2, v0
	s_ashr_i32 s4, s2, 3
	s_and_b32 s2, s4, -8
	s_add_i32 s6, s2, s97
	s_min_i32 s2, s6, 0x4000
	s_ashr_i32 s2, s2, 12
	s_add_i32 s2, s2, 5
	s_mul_hi_i32 s3, s2, 0xc000
	s_mul_i32 s2, s2, 0xc000
	v_and_b32_e32 v70, 63, v0
	s_waitcnt lgkmcnt(0)
	s_add_u32 s2, s54, s2
	s_addc_u32 s3, s55, s3
	v_lshlrev_b32_e32 v64, 4, v70
	v_mov_b32_e32 v65, 0
	v_lshl_add_u64 v[0:1], s[2:3], 0, v[64:65]
	s_mov_b64 s[2:3], 0x10a000
	v_lshl_add_u64 v[36:37], v[0:1], 0, s[2:3]
	s_mov_b32 s2, 0x10b000
	v_add_co_u32_e32 v66, vcc, s2, v0
	v_lshl_add_u64 v[38:39], s[0:1], 0, v[64:65]
	s_nop 0
	v_addc_co_u32_e32 v67, vcc, 0, v1, vcc
	global_load_dwordx4 v[0:3], v64, s[0:1]
	global_load_dwordx4 v[4:7], v64, s[0:1] offset:1024
	global_load_dwordx4 v[8:11], v[36:37], off offset:1024
	global_load_dwordx4 v[12:15], v[36:37], off offset:2048
	global_load_dwordx4 v[16:19], v[36:37], off offset:3072
	global_load_dwordx4 v[20:23], v64, s[0:1] offset:2048
	global_load_dwordx4 v[24:27], v64, s[0:1] offset:3072
	global_load_dwordx4 v[28:31], v[66:67], off offset:-4096
	global_load_dwordx4 v[32:35], v[66:67], off
	s_movk_i32 s0, 0x1000
	v_add_co_u32_e32 v68, vcc, s0, v38
	v_readlane_b32 s0, v251, 14
	s_nop 0
	v_addc_co_u32_e32 v69, vcc, 0, v39, vcc
	global_load_dwordx4 v[36:39], v[68:69], off
	global_load_dwordx4 v[40:43], v[68:69], off offset:1024
	global_load_dwordx4 v[44:47], v[66:67], off offset:1024
	global_load_dwordx4 v[48:51], v[66:67], off offset:2048
	global_load_dwordx4 v[52:55], v[66:67], off offset:3072
	global_load_dwordx4 v[56:59], v[68:69], off offset:2048
	global_load_dwordx4 v[60:63], v[68:69], off offset:3072
	v_lshlrev_b32_e32 v66, 2, v70
	v_mov_b32_e32 v67, v65
	v_readlane_b32 s1, v251, 15
	s_or_b32 s5, s6, 7
	s_add_i32 s8, s6, -1
	v_lshl_add_u64 v[66:67], s[0:1], 0, v[66:67]
	s_lshl_b32 s0, s4, 2
	s_andn2_b32 s0, s0, 31
	s_add_i32 s0, s27, s0
	s_ashr_i32 s1, s0, 31
	s_lshl_b64 s[0:1], s[0:1], 2
	s_add_u32 s9, s0, 0x400000
	s_addc_u32 s10, s1, 0
	s_ashr_i32 s7, s6, 31
	s_lshl_b64 s[0:1], s[6:7], 13
	s_add_u32 s0, s52, s0
	s_addc_u32 s1, s53, s1
	v_lshl_add_u64 v[68:69], s[0:1], 0, v[64:65]
	s_mov_b64 s[2:3], 0x1000
	s_lshl_b64 s[0:1], s[6:7], 12
	v_lshl_add_u64 v[68:69], v[68:69], 0, s[2:3]
	v_lshl_or_b32 v70, v70, 3, s0
	v_mov_b32_e32 v71, s1
	s_mov_b32 s4, 0x3d800000
	v_mov_b32_e32 v64, 0x358637bd
	s_mov_b32 s11, 0xf800000
	v_mov_b32_e32 v74, 0x260
	s_mov_b64 s[6:7], 0x2000
	s_add_u32 s0, s54, s9
	s_addc_u32 s1, s55, s10
	global_load_dwordx4 v[234:237], v65, s[0:1]
.LBB0_1569:
	s_add_u32 s0, s54, s9
	s_addc_u32 s1, s55, s10
	v_lshl_add_u64 v[72:73], s[54:55], 0, v[70:71]
	v_add_co_u32_e32 v72, vcc, 0x34800000, v72
	s_add_i32 s8, s8, 1
	s_nop 0
	v_addc_co_u32_e32 v73, vcc, 0, v73, vcc
	global_load_dwordx2 v[80:81], v[72:73], off
	global_load_dwordx2 v[82:83], v[72:73], off offset:512
	global_load_dwordx2 v[84:85], v[72:73], off offset:1024
	global_load_dwordx2 v[86:87], v[72:73], off offset:1536
	global_load_dwordx2 v[88:89], v[72:73], off offset:2048
	global_load_dwordx2 v[90:91], v[72:73], off offset:2560
	global_load_dwordx2 v[92:93], v[72:73], off offset:3072
	global_load_dwordx2 v[94:95], v[72:73], off offset:3584
	s_add_u32 s9, s9, 16
	s_addc_u32 s10, s10, 0
	v_lshl_add_u64 v[70:71], v[70:71], 0, s[2:3]
	s_cmp_lt_i32 s8, s5
	s_waitcnt vmcnt(8)
	v_mov_b32_e32 v76, v234
	v_mov_b32_e32 v77, v235
	v_mov_b32_e32 v78, v236
	v_mov_b32_e32 v79, v237
	global_load_dwordx4 v[234:237], v65, s[0:1] offset:16
	v_ashrrev_i32_e32 v73, 31, v76
	v_mov_b32_e32 v72, v76
	v_ashrrev_i32_e32 v97, 31, v77
	v_mov_b32_e32 v96, v77
	v_ashrrev_i32_e32 v77, 31, v78
	v_mov_b32_e32 v76, v78
	v_ashrrev_i32_e32 v99, 31, v79
	v_mov_b32_e32 v98, v79
	v_lshlrev_b64 v[72:73], 11, v[72:73]
	v_lshlrev_b64 v[96:97], 11, v[96:97]
	v_lshlrev_b64 v[76:77], 11, v[76:77]
	v_lshlrev_b64 v[98:99], 11, v[98:99]
	v_lshl_add_u64 v[72:73], v[66:67], 0, v[72:73]
	v_lshl_add_u64 v[96:97], v[66:67], 0, v[96:97]
	v_lshl_add_u64 v[76:77], v[66:67], 0, v[76:77]
	v_lshl_add_u64 v[98:99], v[66:67], 0, v[98:99]
	global_load_dword v75, v[72:73], off
	global_load_dword v114, v[72:73], off offset:256
	global_load_dword v116, v[72:73], off offset:512
	global_load_dword v120, v[72:73], off offset:768
	global_load_dword v124, v[72:73], off offset:1024
	global_load_dword v128, v[72:73], off offset:1280
	global_load_dword v132, v[72:73], off offset:1536
	global_load_dword v136, v[72:73], off offset:1792
	global_load_dword v140, v[96:97], off
	global_load_dword v144, v[96:97], off offset:256
	global_load_dword v148, v[96:97], off offset:512
	global_load_dword v152, v[96:97], off offset:768
	global_load_dword v156, v[96:97], off offset:1024
	global_load_dword v160, v[96:97], off offset:1280
	global_load_dword v164, v[96:97], off offset:1536
	global_load_dword v168, v[96:97], off offset:1792
	global_load_dword v172, v[76:77], off
	global_load_dword v176, v[76:77], off offset:256
	global_load_dword v180, v[76:77], off offset:512
	global_load_dword v184, v[76:77], off offset:768
	global_load_dword v188, v[76:77], off offset:1024
	global_load_dword v192, v[76:77], off offset:1280
	global_load_dword v196, v[76:77], off offset:1536
	global_load_dword v200, v[76:77], off offset:1792
	global_load_dword v204, v[98:99], off
	global_load_dword v208, v[98:99], off offset:256
	global_load_dword v212, v[98:99], off offset:512
	global_load_dword v216, v[98:99], off offset:768
	global_load_dword v220, v[98:99], off offset:1024
	global_load_dword v224, v[98:99], off offset:1280
	global_load_dword v228, v[98:99], off offset:1536
	global_load_dword v232, v[98:99], off offset:1792
	s_waitcnt vmcnt(39)
	v_lshlrev_b32_e32 v78, 16, v80
	v_and_b32_e32 v79, 0xffff0000, v80
	v_lshlrev_b32_e32 v80, 16, v81
	v_and_b32_e32 v81, 0xffff0000, v81
	s_waitcnt vmcnt(38)
	v_lshlrev_b32_e32 v100, 16, v82
	v_and_b32_e32 v101, 0xffff0000, v82
	v_lshlrev_b32_e32 v82, 16, v83
	v_and_b32_e32 v83, 0xffff0000, v83
	s_waitcnt vmcnt(37)
	v_lshlrev_b32_e32 v102, 16, v84
	v_and_b32_e32 v103, 0xffff0000, v84
	v_lshlrev_b32_e32 v84, 16, v85
	v_and_b32_e32 v85, 0xffff0000, v85
	s_waitcnt vmcnt(36)
	v_lshlrev_b32_e32 v104, 16, v86
	v_and_b32_e32 v105, 0xffff0000, v86
	s_waitcnt vmcnt(34)
	v_lshlrev_b32_e32 v108, 16, v90
	v_and_b32_e32 v109, 0xffff0000, v90
	s_waitcnt vmcnt(32)
	v_lshlrev_b32_e32 v112, 16, v94
	v_and_b32_e32 v113, 0xffff0000, v94
	v_lshlrev_b32_e32 v106, 16, v88
	v_and_b32_e32 v107, 0xffff0000, v88
	v_lshlrev_b32_e32 v110, 16, v92
	v_and_b32_e32 v111, 0xffff0000, v92
	v_lshlrev_b32_e32 v86, 16, v87
	v_and_b32_e32 v87, 0xffff0000, v87
	v_lshlrev_b32_e32 v88, 16, v89
	v_and_b32_e32 v89, 0xffff0000, v89
	v_lshlrev_b32_e32 v90, 16, v91
	v_and_b32_e32 v91, 0xffff0000, v91
	v_lshlrev_b32_e32 v92, 16, v93
	v_and_b32_e32 v93, 0xffff0000, v93
	v_lshlrev_b32_e32 v94, 16, v95
	v_and_b32_e32 v95, 0xffff0000, v95
	s_waitcnt vmcnt(31)
	v_cvt_pk_f32_fp8_e32 v[72:73], v75
	v_cvt_pk_f32_fp8_sdwa v[76:77], v75 src0_sel:WORD_1
	s_waitcnt vmcnt(30)
	v_cvt_pk_f32_fp8_e32 v[96:97], v114
	v_cvt_pk_f32_fp8_sdwa v[98:99], v114 src0_sel:WORD_1
	s_waitcnt vmcnt(29)
	v_cvt_pk_f32_fp8_e32 v[114:115], v116
	v_cvt_pk_f32_fp8_sdwa v[116:117], v116 src0_sel:WORD_1
	s_waitcnt vmcnt(28)
	v_cvt_pk_f32_fp8_e32 v[118:119], v120
	s_waitcnt vmcnt(26)
	v_cvt_pk_f32_fp8_e32 v[126:127], v128
	s_waitcnt vmcnt(24)
	v_cvt_pk_f32_fp8_e32 v[134:135], v136
	s_waitcnt vmcnt(23)
	v_cvt_pk_f32_fp8_e32 v[138:139], v140
	v_cvt_pk_f32_fp8_sdwa v[140:141], v140 src0_sel:WORD_1
	s_waitcnt vmcnt(22)
	v_cvt_pk_f32_fp8_e32 v[142:143], v144
	v_cvt_pk_f32_fp8_sdwa v[144:145], v144 src0_sel:WORD_1
	v_cvt_pk_f32_fp8_e32 v[122:123], v124
	v_cvt_pk_f32_fp8_e32 v[130:131], v132
	s_waitcnt vmcnt(21)
	v_cvt_pk_f32_fp8_e32 v[146:147], v148
	v_cvt_pk_f32_fp8_sdwa v[148:149], v148 src0_sel:WORD_1
	s_waitcnt vmcnt(20)
	v_cvt_pk_f32_fp8_e32 v[150:151], v152
	s_waitcnt vmcnt(18)
	v_cvt_pk_f32_fp8_e32 v[158:159], v160
	s_waitcnt vmcnt(16)
	v_cvt_pk_f32_fp8_e32 v[166:167], v168
	s_waitcnt vmcnt(15)
	v_cvt_pk_f32_fp8_e32 v[170:171], v172
	v_cvt_pk_f32_fp8_sdwa v[172:173], v172 src0_sel:WORD_1
	s_waitcnt vmcnt(14)
	v_cvt_pk_f32_fp8_e32 v[174:175], v176
	v_cvt_pk_f32_fp8_sdwa v[176:177], v176 src0_sel:WORD_1
	v_cvt_pk_f32_fp8_sdwa v[120:121], v120 src0_sel:WORD_1
	v_cvt_pk_f32_fp8_e32 v[154:155], v156
	v_cvt_pk_f32_fp8_e32 v[162:163], v164
	s_waitcnt vmcnt(13)
	v_cvt_pk_f32_fp8_e32 v[178:179], v180
	v_cvt_pk_f32_fp8_sdwa v[180:181], v180 src0_sel:WORD_1
	s_waitcnt vmcnt(12)
	v_cvt_pk_f32_fp8_e32 v[182:183], v184
	s_waitcnt vmcnt(10)
	v_cvt_pk_f32_fp8_e32 v[190:191], v192
	s_waitcnt vmcnt(8)
	v_cvt_pk_f32_fp8_e32 v[198:199], v200
	s_waitcnt vmcnt(7)
	v_cvt_pk_f32_fp8_e32 v[202:203], v204
	v_cvt_pk_f32_fp8_sdwa v[204:205], v204 src0_sel:WORD_1
	s_waitcnt vmcnt(6)
	v_cvt_pk_f32_fp8_e32 v[206:207], v208
	v_cvt_pk_f32_fp8_sdwa v[208:209], v208 src0_sel:WORD_1
	v_cvt_pk_f32_fp8_sdwa v[124:125], v124 src0_sel:WORD_1
	v_cvt_pk_f32_fp8_sdwa v[152:153], v152 src0_sel:WORD_1
	v_cvt_pk_f32_fp8_e32 v[186:187], v188
	v_cvt_pk_f32_fp8_e32 v[194:195], v196
	s_waitcnt vmcnt(5)
	v_cvt_pk_f32_fp8_e32 v[210:211], v212
	v_cvt_pk_f32_fp8_sdwa v[212:213], v212 src0_sel:WORD_1
	s_waitcnt vmcnt(4)
	v_cvt_pk_f32_fp8_e32 v[214:215], v216
	s_waitcnt vmcnt(2)
	v_cvt_pk_f32_fp8_e32 v[222:223], v224
	s_waitcnt vmcnt(0)
	v_cvt_pk_f32_fp8_e32 v[230:231], v232
	v_pk_add_f32 v[72:73], v[72:73], 0 op_sel_hi:[1,0]
	v_pk_add_f32 v[76:77], v[76:77], 0 op_sel_hi:[1,0]
	v_pk_add_f32 v[96:97], v[96:97], 0 op_sel_hi:[1,0]
	v_pk_add_f32 v[98:99], v[98:99], 0 op_sel_hi:[1,0]
	v_cvt_pk_f32_fp8_sdwa v[128:129], v128 src0_sel:WORD_1
	v_cvt_pk_f32_fp8_sdwa v[132:133], v132 src0_sel:WORD_1
	v_cvt_pk_f32_fp8_sdwa v[156:157], v156 src0_sel:WORD_1
	v_cvt_pk_f32_fp8_sdwa v[184:185], v184 src0_sel:WORD_1
	v_cvt_pk_f32_fp8_e32 v[218:219], v220
	v_cvt_pk_f32_fp8_e32 v[226:227], v228
	v_pk_add_f32 v[116:117], v[116:117], 0 op_sel_hi:[1,0]
	v_pk_add_f32 v[114:115], v[114:115], 0 op_sel_hi:[1,0]
	v_pk_add_f32 v[118:119], v[118:119], 0 op_sel_hi:[1,0]
	v_pk_add_f32 v[126:127], v[126:127], 0 op_sel_hi:[1,0]
	v_pk_add_f32 v[134:135], v[134:135], 0 op_sel_hi:[1,0]
	v_pk_add_f32 v[76:77], v[76:77], v[140:141]
	v_pk_add_f32 v[72:73], v[72:73], v[138:139]
	v_pk_add_f32 v[98:99], v[98:99], v[144:145]
	v_pk_add_f32 v[96:97], v[96:97], v[142:143]
	v_cvt_pk_f32_fp8_sdwa v[160:161], v160 src0_sel:WORD_1
	v_cvt_pk_f32_fp8_sdwa v[164:165], v164 src0_sel:WORD_1
	v_cvt_pk_f32_fp8_sdwa v[188:189], v188 src0_sel:WORD_1
	v_cvt_pk_f32_fp8_sdwa v[216:217], v216 src0_sel:WORD_1
	v_pk_add_f32 v[122:123], v[122:123], 0 op_sel_hi:[1,0]
	v_pk_add_f32 v[130:131], v[130:131], 0 op_sel_hi:[1,0]
	v_pk_add_f32 v[114:115], v[114:115], v[146:147]
	v_pk_add_f32 v[116:117], v[116:117], v[148:149]
	v_pk_add_f32 v[118:119], v[118:119], v[150:151]
	v_pk_add_f32 v[126:127], v[126:127], v[158:159]
	v_pk_add_f32 v[134:135], v[134:135], v[166:167]
	v_pk_add_f32 v[72:73], v[72:73], v[170:171]
	v_pk_add_f32 v[76:77], v[76:77], v[172:173]
	v_pk_add_f32 v[96:97], v[96:97], v[174:175]
	v_pk_add_f32 v[98:99], v[98:99], v[176:177]
	v_cvt_pk_f32_fp8_sdwa v[192:193], v192 src0_sel:WORD_1
	v_cvt_pk_f32_fp8_sdwa v[196:197], v196 src0_sel:WORD_1
	v_cvt_pk_f32_fp8_sdwa v[220:221], v220 src0_sel:WORD_1
	v_pk_add_f32 v[120:121], v[120:121], 0 op_sel_hi:[1,0]
	v_pk_add_f32 v[122:123], v[122:123], v[154:155]
	v_pk_add_f32 v[130:131], v[130:131], v[162:163]
	v_pk_add_f32 v[116:117], v[116:117], v[180:181]
	v_pk_add_f32 v[114:115], v[114:115], v[178:179]
	v_pk_add_f32 v[118:119], v[118:119], v[182:183]
	v_pk_add_f32 v[126:127], v[126:127], v[190:191]
	v_pk_add_f32 v[134:135], v[134:135], v[198:199]
	v_pk_add_f32 v[76:77], v[76:77], v[204:205]
	v_pk_add_f32 v[72:73], v[72:73], v[202:203]
	v_pk_add_f32 v[98:99], v[98:99], v[208:209]
	v_pk_add_f32 v[96:97], v[96:97], v[206:207]
	v_cvt_pk_f32_fp8_sdwa v[136:137], v136 src0_sel:WORD_1
	v_cvt_pk_f32_fp8_sdwa v[224:225], v224 src0_sel:WORD_1
	v_cvt_pk_f32_fp8_sdwa v[228:229], v228 src0_sel:WORD_1
	v_pk_add_f32 v[124:125], v[124:125], 0 op_sel_hi:[1,0]
	v_pk_add_f32 v[120:121], v[120:121], v[152:153]
	v_pk_add_f32 v[122:123], v[122:123], v[186:187]
	v_pk_add_f32 v[130:131], v[130:131], v[194:195]
	v_pk_add_f32 v[114:115], v[114:115], v[210:211]
	v_pk_add_f32 v[116:117], v[116:117], v[212:213]
	v_pk_add_f32 v[118:119], v[118:119], v[214:215]
	v_pk_add_f32 v[126:127], v[126:127], v[222:223]
	v_pk_add_f32 v[134:135], v[134:135], v[230:231]
	v_pk_mul_f32 v[72:73], v[28:29], v[72:73]
	v_pk_mul_f32 v[76:77], v[30:31], v[76:77]
	v_pk_mul_f32 v[96:97], v[8:9], v[96:97]
	v_pk_mul_f32 v[98:99], v[10:11], v[98:99]
	v_cvt_pk_f32_fp8_sdwa v[168:169], v168 src0_sel:WORD_1
	v_pk_add_f32 v[128:129], v[128:129], 0 op_sel_hi:[1,0]
	v_pk_add_f32 v[132:133], v[132:133], 0 op_sel_hi:[1,0]
	v_pk_add_f32 v[124:125], v[124:125], v[156:157]
	v_pk_add_f32 v[120:121], v[120:121], v[184:185]
	v_pk_add_f32 v[122:123], v[122:123], v[218:219]
	v_pk_add_f32 v[130:131], v[130:131], v[226:227]
	v_pk_mul_f32 v[116:117], v[14:15], v[116:117]
	v_pk_mul_f32 v[114:115], v[12:13], v[114:115]
	v_pk_mul_f32 v[118:119], v[16:17], v[118:119]
	v_pk_mul_f32 v[126:127], v[44:45], v[126:127]
	v_pk_mul_f32 v[134:135], v[52:53], v[134:135]
	v_pk_fma_f32 v[76:77], v[76:77], s[4:5], v[80:81] op_sel_hi:[1,0,1]
	v_pk_fma_f32 v[72:73], v[72:73], s[4:5], v[78:79] op_sel_hi:[1,0,1]
	v_pk_fma_f32 v[78:79], v[98:99], s[4:5], v[82:83] op_sel_hi:[1,0,1]
	v_pk_fma_f32 v[80:81], v[96:97], s[4:5], v[100:101] op_sel_hi:[1,0,1]
	v_cvt_pk_f32_fp8_sdwa v[200:201], v200 src0_sel:WORD_1
	v_pk_add_f32 v[128:129], v[128:129], v[160:161]
	v_pk_add_f32 v[132:133], v[132:133], v[164:165]
	v_pk_add_f32 v[124:125], v[124:125], v[188:189]
	v_pk_add_f32 v[120:121], v[120:121], v[216:217]
	v_pk_mul_f32 v[122:123], v[32:33], v[122:123]
	v_pk_mul_f32 v[130:131], v[48:49], v[130:131]
	v_pk_fma_f32 v[82:83], v[114:115], s[4:5], v[102:103] op_sel_hi:[1,0,1]
	v_pk_fma_f32 v[84:85], v[116:117], s[4:5], v[84:85] op_sel_hi:[1,0,1]
	v_pk_fma_f32 v[96:97], v[118:119], s[4:5], v[104:105] op_sel_hi:[1,0,1]
	v_pk_fma_f32 v[100:101], v[126:127], s[4:5], v[108:109] op_sel_hi:[1,0,1]
	v_pk_fma_f32 v[104:105], v[134:135], s[4:5], v[112:113] op_sel_hi:[1,0,1]
	v_mov_b32_e32 v108, v73
	v_mov_b32_e32 v109, v81
	v_mov_b32_e32 v112, v77
	v_mov_b32_e32 v113, v79
	v_cvt_pk_f32_fp8_sdwa v[232:233], v232 src0_sel:WORD_1
	v_pk_add_f32 v[128:129], v[128:129], v[192:193]
	v_pk_add_f32 v[132:133], v[132:133], v[196:197]
	v_pk_add_f32 v[124:125], v[124:125], v[220:221]
	v_pk_mul_f32 v[120:121], v[18:19], v[120:121]
	v_pk_fma_f32 v[98:99], v[122:123], s[4:5], v[106:107] op_sel_hi:[1,0,1]
	v_pk_fma_f32 v[102:103], v[130:131], s[4:5], v[110:111] op_sel_hi:[1,0,1]
	v_mov_b32_e32 v106, v72
	v_mov_b32_e32 v107, v80
	v_mov_b32_e32 v110, v76
	v_mov_b32_e32 v111, v78
	v_pk_mul_f32 v[114:115], v[84:85], v[84:85]
	v_pk_mul_f32 v[116:117], v[82:83], v[82:83]
	v_pk_mul_f32 v[108:109], v[108:109], v[108:109]
	v_pk_mul_f32 v[112:113], v[112:113], v[112:113]
	v_pk_add_f32 v[136:137], v[136:137], 0 op_sel_hi:[1,0]
	v_pk_add_f32 v[128:129], v[128:129], v[224:225]
	v_pk_add_f32 v[132:133], v[132:133], v[228:229]
	v_pk_mul_f32 v[124:125], v[34:35], v[124:125]
	v_pk_fma_f32 v[86:87], v[120:121], s[4:5], v[86:87] op_sel_hi:[1,0,1]
	v_pk_mov_b32 v[130:131], v[116:117], v[114:115] op_sel:[1,0]
	v_mov_b32_e32 v117, v115
	v_pk_fma_f32 v[106:107], v[106:107], v[106:107], v[108:109]
	v_pk_fma_f32 v[108:109], v[110:111], v[110:111], v[112:113]
	v_pk_add_f32 v[136:137], v[136:137], v[168:169]
	v_pk_mul_f32 v[128:129], v[46:47], v[128:129]
	v_pk_mul_f32 v[132:133], v[50:51], v[132:133]
	v_pk_fma_f32 v[88:89], v[124:125], s[4:5], v[88:89] op_sel_hi:[1,0,1]
	v_mul_f32_e32 v118, v97, v97
	v_mul_f32_e32 v120, v87, v87
	v_pk_add_f32 v[110:111], v[130:131], v[116:117]
	v_pk_add_f32 v[106:107], v[106:107], v[108:109]
	v_pk_add_f32 v[136:137], v[136:137], v[200:201]
	v_pk_fma_f32 v[90:91], v[128:129], s[4:5], v[90:91] op_sel_hi:[1,0,1]
	v_pk_fma_f32 v[92:93], v[132:133], s[4:5], v[92:93] op_sel_hi:[1,0,1]
	v_mul_f32_e32 v75, v98, v98
	v_mul_f32_e32 v129, v99, v99
	v_mul_f32_e32 v132, v88, v88
	v_mul_f32_e32 v133, v89, v89
	v_pk_fma_f32 v[114:115], v[96:97], v[96:97], v[118:119] op_sel_hi:[1,1,0]
	v_pk_fma_f32 v[118:119], v[86:87], v[86:87], v[120:121] op_sel_hi:[1,1,0]
	v_pk_add_f32 v[108:109], v[110:111], v[110:111] op_sel:[0,1] op_sel_hi:[1,0]
	v_pk_add_f32 v[106:107], v[106:107], v[106:107] op_sel:[0,1] op_sel_hi:[1,0]
	v_pk_add_f32 v[136:137], v[136:137], v[232:233]
	v_pk_mul_f32 v[122:123], v[90:91], v[90:91]
	v_pk_mul_f32 v[124:125], v[100:101], v[100:101]
	v_mov_b32_e32 v115, v132
	v_mov_b32_e32 v119, v133
	v_mov_b32_e32 v109, v129
	v_mov_b32_e32 v107, v75
	v_pk_mul_f32 v[136:137], v[54:55], v[136:137]
	v_pk_mov_b32 v[120:121], v[124:125], v[122:123] op_sel:[1,0]
	v_mov_b32_e32 v125, v123
	v_pk_add_f32 v[110:111], v[114:115], v[118:119]
	v_pk_add_f32 v[106:107], v[106:107], v[108:109]
	v_pk_fma_f32 v[94:95], v[136:137], s[4:5], v[94:95] op_sel_hi:[1,0,1]
	v_mul_f32_e32 v126, v103, v103
	v_mul_f32_e32 v128, v93, v93
	v_pk_add_f32 v[112:113], v[120:121], v[124:125]
	v_pk_add_f32 v[106:107], v[106:107], v[110:111]
	v_mul_f32_e32 v134, v104, v104
	v_mul_f32_e32 v135, v105, v105
	v_mul_f32_e32 v136, v94, v94
	v_mul_f32_e32 v137, v95, v95
	v_pk_fma_f32 v[122:123], v[102:103], v[102:103], v[126:127] op_sel_hi:[1,1,0]
	v_pk_fma_f32 v[126:127], v[92:93], v[92:93], v[128:129] op_sel_hi:[1,1,0]
	v_pk_add_f32 v[112:113], v[112:113], v[112:113] op_sel:[0,1] op_sel_hi:[1,0]
	v_pk_add_f32 v[106:107], v[106:107], v[106:107] op_sel:[0,1] op_sel_hi:[1,0]
	v_mov_b32_e32 v123, v136
	v_mov_b32_e32 v127, v137
	v_mov_b32_e32 v113, v135
	v_mov_b32_e32 v107, v134
	v_pk_add_f32 v[114:115], v[122:123], v[126:127]
	v_pk_add_f32 v[106:107], v[106:107], v[112:113]
	s_nop 0
	v_pk_add_f32 v[106:107], v[106:107], v[114:115]
	s_nop 0
	v_add_f32_e32 v75, v106, v107
	s_nop 1
	v_add_f32_dpp v75, v75, v75 quad_perm:[1,0,3,2] row_mask:0xf bank_mask:0xf bound_ctrl:1
	s_nop 1
	v_add_f32_dpp v75, v75, v75 quad_perm:[2,3,0,1] row_mask:0xf bank_mask:0xf bound_ctrl:1
	s_nop 1
	v_add_f32_dpp v75, v75, v75 row_half_mirror row_mask:0xf bank_mask:0xf bound_ctrl:1
	s_nop 1
	v_add_f32_dpp v75, v75, v75 row_mirror row_mask:0xf bank_mask:0xf bound_ctrl:1
	s_nop 0
	v_readlane_b32 s12, v75, 16
	v_readlane_b32 s13, v75, 48
	v_readlane_b32 s0, v75, 0
	v_readlane_b32 s1, v75, 32
	v_mov_b32_e32 v106, s12
	v_mov_b32_e32 v107, s13
	v_pk_add_f32 v[106:107], s[0:1], v[106:107]
	s_nop 0
	v_add_f32_e32 v75, v106, v107
	v_fmamk_f32 v75, v75, 0x3a000000, v64
	v_mul_f32_e32 v106, 0x4f800000, v75
	v_cmp_gt_f32_e32 vcc, s11, v75
	s_nop 1
	v_cndmask_b32_e32 v75, v75, v106, vcc
	v_sqrt_f32_e32 v106, v75
	s_nop 0
	v_add_u32_e32 v107, -1, v106
	v_add_u32_e32 v108, 1, v106
	v_fma_f32 v109, -v107, v106, v75
	v_fma_f32 v110, -v108, v106, v75
	v_cmp_ge_f32_e64 s[0:1], 0, v109
	s_nop 1
	v_cndmask_b32_e64 v106, v106, v107, s[0:1]
	v_cmp_lt_f32_e64 s[0:1], 0, v110
	s_nop 1
	v_cndmask_b32_e64 v106, v106, v108, s[0:1]
	v_mul_f32_e32 v107, 0x37800000, v106
	v_cndmask_b32_e32 v106, v106, v107, vcc
	v_cmp_class_f32_e32 vcc, v75, v74
	s_nop 1
	v_cndmask_b32_e32 v75, v106, v75, vcc
	v_div_scale_f32 v106, s[0:1], v75, v75, 1.0
	v_rcp_f32_e32 v108, v106
	v_div_scale_f32 v107, vcc, 1.0, v75, 1.0
	v_fma_f32 v109, -v106, v108, 1.0
	v_fmac_f32_e32 v108, v109, v108
	v_mul_f32_e32 v109, v107, v108
	v_fma_f32 v110, -v106, v109, v107
	v_fmac_f32_e32 v109, v110, v108
	v_fma_f32 v106, -v106, v109, v107
	v_div_fmas_f32 v106, v106, v108, v109
	v_div_fixup_f32 v106, v106, v75, 1.0
	v_pk_mul_f32 v[72:73], v[72:73], v[106:107] op_sel_hi:[1,0]
	v_pk_mul_f32 v[76:77], v[76:77], v[106:107] op_sel_hi:[1,0]
	v_pk_mul_f32 v[80:81], v[80:81], v[106:107] op_sel_hi:[1,0]
	v_pk_mul_f32 v[108:109], v[78:79], v[106:107] op_sel_hi:[1,0]
	v_pk_mul_f32 v[110:111], v[82:83], v[106:107] op_sel_hi:[1,0]
	v_pk_mul_f32 v[84:85], v[84:85], v[106:107] op_sel_hi:[1,0]
	v_pk_mul_f32 v[96:97], v[96:97], v[106:107] op_sel_hi:[1,0]
	v_pk_mul_f32 v[112:113], v[86:87], v[106:107] op_sel_hi:[1,0]
	v_pk_mul_f32 v[98:99], v[98:99], v[106:107] op_sel_hi:[1,0]
	v_pk_mul_f32 v[114:115], v[88:89], v[106:107] op_sel_hi:[1,0]
	v_pk_mul_f32 v[100:101], v[100:101], v[106:107] op_sel_hi:[1,0]
	v_pk_mul_f32 v[116:117], v[90:91], v[106:107] op_sel_hi:[1,0]
	v_pk_mul_f32 v[118:119], v[102:103], v[106:107] op_sel_hi:[1,0]
	v_pk_mul_f32 v[102:103], v[92:93], v[106:107] op_sel_hi:[1,0]
	v_pk_mul_f32 v[104:105], v[104:105], v[106:107] op_sel_hi:[1,0]
	v_pk_mul_f32 v[106:107], v[94:95], v[106:107] op_sel_hi:[1,0]
	v_pk_mul_f32 v[78:79], v[2:3], v[76:77]
	v_pk_mul_f32 v[76:77], v[0:1], v[72:73]
	v_pk_mul_f32 v[82:83], v[6:7], v[108:109]
	v_pk_mul_f32 v[80:81], v[4:5], v[80:81]
	v_pk_mul_f32 v[86:87], v[22:23], v[84:85]
	v_pk_mul_f32 v[84:85], v[20:21], v[110:111]
	v_pk_mul_f32 v[90:91], v[26:27], v[112:113]
	v_pk_mul_f32 v[88:89], v[24:25], v[96:97]
	v_pk_mul_f32 v[94:95], v[38:39], v[114:115]
	v_pk_mul_f32 v[92:93], v[36:37], v[98:99]
	v_pk_mul_f32 v[98:99], v[42:43], v[116:117]
	v_pk_mul_f32 v[96:97], v[40:41], v[100:101]
	v_pk_mul_f32 v[102:103], v[58:59], v[102:103]
	v_pk_mul_f32 v[100:101], v[56:57], v[118:119]
	v_pk_mul_f32 v[106:107], v[62:63], v[106:107]
	v_pk_mul_f32 v[104:105], v[60:61], v[104:105]
	global_store_dwordx4 v[68:69], v[76:79], off offset:-4096
	global_store_dwordx4 v[68:69], v[80:83], off offset:-3072
	global_store_dwordx4 v[68:69], v[84:87], off offset:-2048
	global_store_dwordx4 v[68:69], v[88:91], off offset:-1024
	global_store_dwordx4 v[68:69], v[92:95], off
	global_store_dwordx4 v[68:69], v[96:99], off offset:1024
	global_store_dwordx4 v[68:69], v[100:103], off offset:2048
	global_store_dwordx4 v[68:69], v[104:107], off offset:3072
	v_lshl_add_u64 v[68:69], v[68:69], 0, s[6:7]
	s_cbranch_scc1 .LBB0_1569
